# di7_nop4
# baseline (speedup 1.0000x reference)
_Z11main_kernelPKfPKhS0_S0_Pf:
	s_ashr_i32 s38, s2, 2
	v_readfirstlane_b32 s3, v0
	s_and_b32 s37, s2, 7
	s_and_b32 s12, s38, 0xfffff8
	s_lshr_b32 s36, s3, 7
	s_or_b32 s12, s12, s37
	s_lshr_b32 s44, s12, 3
	s_lshl_b32 s44, s44, 1
	s_and_b32 s50, s12, 1
	s_or_b32 s44, s44, s50
	s_and_b32 s44, s44, 15
	s_lshl_b32 s48, s44, 15
	s_lshl_b32 s44, s44, 8
	s_add_i32 s46, s44, 0x100
	s_add_i32 s49, s44, 0x200
	s_bfe_u32 s31, s3, 0x10006
	s_lshl_b32 s12, s12, 8
	s_lshl_b32 s33, s36, 6
	s_load_dwordx8 s[4:11], s[0:1], 0x0
	s_add_i32 s28, s33, s12
	s_lshl_b32 s34, s31, 5
	s_or_b32 s12, s28, s34
	s_lshr_b32 s30, s3, 6
	s_lshl_b32 s39, s12, 12
	s_cmpk_gt_u32 s3, 0xff
	v_lshlrev_b32_e32 v2, 3, v0
	s_cselect_b64 s[24:25], -1, 0
	s_cmpk_lt_u32 s3, 0x100
	v_mov_b32_e32 v3, 0
	s_cselect_b64 s[26:27], -1, 0
	s_mov_b32 s14, 0x200000
	s_bfe_u32 s40, s2, 0x20003
	s_add_i32 s51, s39, s44
	s_and_b32 s52, s46, 0xf00
	s_add_i32 s52, s52, s39
	s_waitcnt lgkmcnt(0)
	s_mov_b32 s41, 0x201000
	s_load_dword s41, s[6:7], s41 offset:0x0
	v_lshl_add_u64 v[4:5], s[6:7], 0, v[2:3]
	v_add_co_u32_e32 v4, vcc, s14, v4
	s_lshl_b32 s29, s40, 8
	s_nop 0
	v_addc_co_u32_e32 v5, vcc, 0, v5, vcc
	v_or_b32_e32 v1, s29, v0
	v_add_lshl_u32 v6, s29, v0, 2
	v_mov_b32_e32 v7, v3
	s_movk_i32 s2, 0xfc00
	s_movk_i32 s12, 0x100
	global_load_dwordx2 v[8:9], v[4:5], off
	v_lshlrev_b32_e32 v4, 2, v1
	v_mov_b32_e32 v5, v3
	v_lshl_add_u64 v[6:7], s[8:9], 0, v[6:7]
	s_mov_b32 s3, -1
	v_lshl_add_u64 v[4:5], s[10:11], 0, v[4:5]
	v_lshl_add_u64 v[6:7], v[6:7], 0, s[2:3]
	v_cmp_gt_u32_e32 vcc, s12, v0
	s_load_dwordx2 s[8:9], s[0:1], 0x20
	v_bfe_u32 v1, v0, 3, 1
	v_cndmask_b32_e32 v5, v7, v5, vcc
	v_cndmask_b32_e32 v4, v6, v4, vcc
	global_load_dword v10, v[4:5], off
	v_lshl_or_b32 v1, s31, 2, v1
	v_and_b32_e32 v198, 15, v0
	v_bfe_u32 v199, v0, 4, 2
	v_mul_u32_u24_e32 v67, 0x440, v1
	v_lshrrev_b32_e32 v1, 1, v0
	v_lshlrev_b32_e32 v200, 4, v198
	v_bfe_u32 v4, v0, 1, 2
	v_bitop3_b32 v1, v199, v1, 3 bitop3:0x78
	s_mul_i32 s10, s36, 0x2200
	s_mov_b32 s15, 0x20000
	s_and_b32 s17, s5, 0xffff
	v_and_b32_e32 v66, 63, v0
	v_lshlrev_b32_e32 v68, 8, v4
	v_lshlrev_b32_e32 v69, 4, v1
	v_and_b32_e32 v70, 8, v2
	v_bitop3_b32 v71, v199, v0, 15 bitop3:0x78
	s_and_b32 s13, s7, 0xffff
	s_mov_b32 s12, s6
	s_mov_b32 s20, s6
	v_lshl_or_b32 v1, v199, 12, v200
	s_brev_b32 s18, 16
	s_mov_b32 s19, s15
	s_mov_b32 s16, s4
	s_mov_b32 s0, s4
	s_mov_b32 s1, s17
	s_add_i32 s10, s10, 0x10000
	s_mov_b32 s35, 0
	s_mov_b32 s21, s13
	s_mov_b32 s22, s14
	s_mov_b32 s23, s15
	s_mov_b32 s2, s18
	s_mov_b32 s3, s15
	s_or_b32 s4, s51, 0x4000
	buffer_load_dwordx4 v[4:7], v1, s[0:3], s51 offen nt sc1
	buffer_load_dwordx4 v[18:21], v1, s[0:3], s4 offen nt sc1
	s_or_b32 s4, s51, 0x8000
	s_or_b32 s5, s51, 0xc000
	buffer_load_dwordx4 v[22:25], v1, s[0:3], s4 offen nt sc1
	buffer_load_dwordx4 v[26:29], v1, s[0:3], s5 offen nt sc1
	s_or_b32 s4, s51, 0x10000
	s_or_b32 s5, s51, 0x14000
	buffer_load_dwordx4 v[34:37], v1, s[0:3], s4 offen nt sc1
	buffer_load_dwordx4 v[42:45], v1, s[0:3], s5 offen nt sc1
	s_or_b32 s4, s51, 0x18000
	s_or_b32 s5, s51, 0x1c000
	buffer_load_dwordx4 v[46:49], v1, s[0:3], s4 offen nt sc1
	buffer_load_dwordx4 v[58:61], v1, s[0:3], s5 offen nt sc1
	s_lshl_b32 s4, s30, 10
	v_lshlrev_b32_e32 v189, 4, v0
	s_lshl_b32 s5, s40, 19
	s_add_i32 s53, s5, s48
	s_mov_b32 m0, s4
	s_or_b32 s11, s53, 0x2000
	buffer_load_dwordx4 v189, s[20:23], s53 offen lds
	s_add_i32 m0, s4, 0x2000
	s_nop 0
	buffer_load_dwordx4 v189, s[20:23], s11 offen lds
	s_add_i32 m0, s4, 0x4000
	s_or_b32 s11, s53, 0x4000
	buffer_load_dwordx4 v189, s[20:23], s11 offen lds
	s_add_i32 m0, s4, 0x6000
	s_or_b32 s11, s53, 0x6000
	buffer_load_dwordx4 v189, s[20:23], s11 offen lds
	s_mov_b32 s20, 0x44800000
	s_waitcnt vmcnt(13)
	v_pk_mul_f32 v[8:9], v[8:9], s[20:21] op_sel_hi:[1,0]
	v_add_u32_e32 v2, 0x21000, v2
	ds_write_b64 v2, v[8:9]
	v_mov_b32_e32 v2, 0x22000
	v_lshl_add_u32 v2, v0, 2, v2
	s_waitcnt vmcnt(12)
	ds_write_b32 v2, v10
	s_waitcnt lgkmcnt(0)
	s_barrier
	s_or_b32 s11, s52, 0x0
	s_or_b32 s20, s52, 0x4000
	buffer_load_dwordx4 v[10:13], v1, s[0:3], s11 offen nt sc1
	buffer_load_dwordx4 v[14:17], v1, s[0:3], s20 offen nt sc1
	s_or_b32 s11, s52, 0x8000
	s_or_b32 s20, s52, 0xc000
	buffer_load_dwordx4 v[30:33], v1, s[0:3], s11 offen nt sc1
	buffer_load_dwordx4 v[38:41], v1, s[0:3], s20 offen nt sc1
	s_or_b32 s11, s52, 0x10000
	s_or_b32 s20, s52, 0x14000
	buffer_load_dwordx4 v[50:53], v1, s[0:3], s11 offen nt sc1
	buffer_load_dwordx4 v[54:57], v1, s[0:3], s20 offen nt sc1
	s_or_b32 s11, s52, 0x18000
	s_or_b32 s20, s52, 0x1c000
	buffer_load_dwordx4 v[74:77], v1, s[0:3], s11 offen nt sc1
	buffer_load_dwordx4 v[78:81], v1, s[0:3], s20 offen nt sc1
	v_or_b32_e32 v162, 0x21000, v200
	v_add_u32_e32 v249, s44, v162
	ds_read_b128 v[62:65], v249
	v_add3_u32 v9, s10, v67, v68
	v_or3_b32 v188, v9, v69, v70
	s_waitcnt vmcnt(19)
	v_cvt_pk_f16_f32 v7, v6, v7
	v_cvt_pk_f16_f32 v6, v4, v5
	s_waitcnt lgkmcnt(0)
	v_cvt_pk_f16_f32 v8, v62, v63
	v_mov_b32_e32 v185, v3
	s_waitcnt vmcnt(18)
	v_cvt_pk_f16_f32 v5, v20, v21
	v_cvt_pk_f16_f32 v4, v18, v19
	v_mov_b32_e32 v184, v3
	v_cvt_pk_f16_f32 v2, v64, v65
	v_dot2c_f32_f16_e32 v185, v6, v8
	v_dot2c_f32_f16_e32 v184, v4, v8
	ds_write2_b64 v188, v[6:7], v[4:5] offset1:8
	s_waitcnt vmcnt(17)
	v_cvt_pk_f16_f32 v4, v22, v23
	v_mov_b32_e32 v183, v3
	s_waitcnt vmcnt(16)
	v_cvt_pk_f16_f32 v6, v26, v27
	v_mov_b32_e32 v181, v3
	v_dot2c_f32_f16_e32 v185, v7, v2
	v_dot2c_f32_f16_e32 v184, v5, v2
	v_cvt_pk_f16_f32 v5, v24, v25
	v_dot2c_f32_f16_e32 v183, v4, v8
	v_cvt_pk_f16_f32 v7, v28, v29
	v_dot2c_f32_f16_e32 v181, v6, v8
	v_dot2c_f32_f16_e32 v183, v5, v2
	v_dot2c_f32_f16_e32 v181, v7, v2
	ds_write2_b64 v188, v[4:5], v[6:7] offset0:16 offset1:24
	s_waitcnt vmcnt(15)
	v_cvt_pk_f16_f32 v5, v36, v37
	v_cvt_pk_f16_f32 v4, v34, v35
	v_mov_b32_e32 v182, v3
	s_waitcnt vmcnt(14)
	v_cvt_pk_f16_f32 v7, v44, v45
	v_cvt_pk_f16_f32 v6, v42, v43
	v_mov_b32_e32 v178, v3
	v_add_u32_e32 v9, 0x800, v188
	v_dot2c_f32_f16_e32 v182, v4, v8
	v_dot2c_f32_f16_e32 v178, v6, v8
	ds_write2_b64 v9, v[4:5], v[6:7] offset0:16 offset1:24
	s_waitcnt vmcnt(13)
	v_cvt_pk_f16_f32 v4, v46, v47
	v_mov_b32_e32 v179, v3
	s_waitcnt vmcnt(12)
	v_cvt_pk_f16_f32 v6, v58, v59
	v_mov_b32_e32 v180, v3
	v_dot2c_f32_f16_e32 v182, v5, v2
	v_dot2c_f32_f16_e32 v178, v7, v2
	v_cvt_pk_f16_f32 v5, v48, v49
	v_dot2c_f32_f16_e32 v179, v4, v8
	v_cvt_pk_f16_f32 v7, v60, v61
	v_dot2c_f32_f16_e32 v180, v6, v8
	v_dot2c_f32_f16_e32 v179, v5, v2
	v_dot2c_f32_f16_e32 v180, v7, v2
	ds_write2_b64 v9, v[4:5], v[6:7] offset0:32 offset1:40
	s_waitcnt vmcnt(8) lgkmcnt(0)
	s_barrier
	s_lshl_b32 s0, s38, 20
	v_lshl_add_u32 v2, v199, 8, s10
	s_and_b32 s0, s0, 0xff800000
	s_lshl_b32 s1, s37, 20
	v_lshl_or_b32 v187, v71, 4, v2
	v_lshlrev_b32_e32 v2, 4, v66
	s_or_b32 s0, s0, s1
	s_lshl_b32 s1, s36, 18
	v_lshl_or_b32 v186, s31, 14, v2
	s_add_i32 s0, s0, s1
	s_lshl_b32 s1, s31, 17
	v_cndmask_b32_e64 v2, 0, 1, s[26:27]
	s_or_b32 s11, s0, s1
	v_or_b32_e32 v163, 0x21100, v200
	s_mov_b32 s10, -1
	v_cmp_ne_u32_e64 s[0:1], 1, v2
	s_mov_b32 s20, 0
	v_mov_b32_e32 v2, v3
	v_mov_b32_e32 v4, v3
	v_mov_b32_e32 v5, v3
	v_mov_b32_e32 v26, v3
	v_mov_b32_e32 v27, v3
	v_mov_b32_e32 v28, v3
	v_mov_b32_e32 v29, v3
	v_mov_b32_e32 v42, v3
	v_mov_b32_e32 v43, v3
	v_mov_b32_e32 v44, v3
	v_mov_b32_e32 v45, v3
	v_mov_b32_e32 v46, v3
	v_mov_b32_e32 v47, v3
	v_mov_b32_e32 v48, v3
	v_mov_b32_e32 v49, v3
	v_mov_b32_e32 v6, v3
	v_mov_b32_e32 v7, v3
	v_mov_b32_e32 v8, v3
	v_mov_b32_e32 v9, v3
	v_mov_b32_e32 v18, v3
	v_mov_b32_e32 v19, v3
	v_mov_b32_e32 v20, v3
	v_mov_b32_e32 v21, v3
	v_mov_b32_e32 v22, v3
	v_mov_b32_e32 v23, v3
	v_mov_b32_e32 v24, v3
	v_mov_b32_e32 v25, v3
	v_mov_b32_e32 v34, v3
	v_mov_b32_e32 v35, v3
	v_mov_b32_e32 v36, v3
	v_mov_b32_e32 v37, v3
	v_mov_b32_e32 v82, v3
	v_mov_b32_e32 v83, v3
	v_mov_b32_e32 v84, v3
	v_mov_b32_e32 v85, v3
	v_mov_b32_e32 v86, v3
	v_mov_b32_e32 v87, v3
	v_mov_b32_e32 v88, v3
	v_mov_b32_e32 v89, v3
	v_mov_b32_e32 v98, v3
	v_mov_b32_e32 v99, v3
	v_mov_b32_e32 v100, v3
	v_mov_b32_e32 v101, v3
	v_mov_b32_e32 v106, v3
	v_mov_b32_e32 v107, v3
	v_mov_b32_e32 v108, v3
	v_mov_b32_e32 v109, v3
	v_mov_b32_e32 v58, v3
	v_mov_b32_e32 v59, v3
	v_mov_b32_e32 v60, v3
	v_mov_b32_e32 v61, v3
	v_mov_b32_e32 v62, v3
	v_mov_b32_e32 v63, v3
	v_mov_b32_e32 v64, v3
	v_mov_b32_e32 v65, v3
	v_mov_b32_e32 v66, v3
	v_mov_b32_e32 v67, v3
	v_mov_b32_e32 v68, v3
	v_mov_b32_e32 v69, v3
	v_mov_b32_e32 v70, v3
	v_mov_b32_e32 v71, v3
	v_mov_b32_e32 v72, v3
	v_mov_b32_e32 v73, v3
	v_mov_b32_e32 v118, v3
	v_mov_b32_e32 v119, v3
	v_mov_b32_e32 v120, v3
	v_mov_b32_e32 v121, v3
	v_mov_b32_e32 v122, v3
	v_mov_b32_e32 v123, v3
	v_mov_b32_e32 v124, v3
	v_mov_b32_e32 v125, v3
	v_mov_b32_e32 v134, v3
	v_mov_b32_e32 v135, v3
	v_mov_b32_e32 v136, v3
	v_mov_b32_e32 v137, v3
	v_mov_b32_e32 v138, v3
	v_mov_b32_e32 v139, v3
	v_mov_b32_e32 v140, v3
	v_mov_b32_e32 v141, v3
	v_mov_b32_e32 v94, v3
	v_mov_b32_e32 v95, v3
	v_mov_b32_e32 v96, v3
	v_mov_b32_e32 v97, v3
	v_mov_b32_e32 v102, v3
	v_mov_b32_e32 v103, v3
	v_mov_b32_e32 v104, v3
	v_mov_b32_e32 v105, v3
	v_mov_b32_e32 v110, v3
	v_mov_b32_e32 v111, v3
	v_mov_b32_e32 v112, v3
	v_mov_b32_e32 v113, v3
	v_mov_b32_e32 v90, v3
	v_mov_b32_e32 v91, v3
	v_mov_b32_e32 v92, v3
	v_mov_b32_e32 v93, v3
	v_mov_b32_e32 v142, v3
	v_mov_b32_e32 v143, v3
	v_mov_b32_e32 v144, v3
	v_mov_b32_e32 v145, v3
	v_mov_b32_e32 v146, v3
	v_mov_b32_e32 v147, v3
	v_mov_b32_e32 v148, v3
	v_mov_b32_e32 v149, v3
	v_mov_b32_e32 v154, v3
	v_mov_b32_e32 v155, v3
	v_mov_b32_e32 v156, v3
	v_mov_b32_e32 v157, v3
	v_mov_b32_e32 v150, v3
	v_mov_b32_e32 v151, v3
	v_mov_b32_e32 v152, v3
	v_mov_b32_e32 v153, v3
	v_mov_b32_e32 v114, v3
	v_mov_b32_e32 v115, v3
	v_mov_b32_e32 v116, v3
	v_mov_b32_e32 v117, v3
	v_mov_b32_e32 v126, v3
	v_mov_b32_e32 v127, v3
	v_mov_b32_e32 v128, v3
	v_mov_b32_e32 v129, v3
	v_mov_b32_e32 v130, v3
	v_mov_b32_e32 v131, v3
	v_mov_b32_e32 v132, v3
	v_mov_b32_e32 v133, v3
	v_mov_b32_e32 v158, v3
	v_mov_b32_e32 v159, v3
	v_mov_b32_e32 v160, v3
	v_mov_b32_e32 v161, v3
	s_add_i32 s22, s10, 2
	s_add_i32 s54, s20, s46
	s_and_b32 s54, s54, 0xf00
	v_add_u32_e32 v164, s54, v162
	s_nop 0
